# final combine phases: nt also on the residual row loads and the f32 output stores
# speedup vs baseline: 1.0225x; 1.0062x over previous
; __device__ __forceinline__ void p_final(const Args& a, const Frame& F, int half) {
;     ...
;         f32x4* xr = (f32x4*)(a.out + (size_t)t * D) + F.lane;
;         const u32x2* x1p = (const u32x2*)x1_row(a.out, a.ws, t) + F.lane;
;         const f32x4* g2 = (const f32x4*)(mod + (t >> 13) * 6144 + 5120) + F.lane;
;         int rk[4]; float wk[4];
; #pragma unroll
;         for (int k = 0; k < 4; ++k) { rk[k] = rkn[k]; wk[k] = wkn[k]; }
;         u32x2 ok[4][4], xw[4];
; #pragma unroll
;         for (int j = 0; j < 4; ++j) { xw[j] = x1p[64 * j];
; #pragma unroll
;             for (int k = 0; k < 4; ++k) ok[j][k] = *((const u32x2*)(OUTK + (size_t)rk[k] * D) + F.lane + 64 * j); }
;         { const int tn = t + NGW; if (tn < tend) {
; #pragma unroll
;             for (int k = 0; k < 4; ++k) { rkn[k] = tok_row[tn * 4 + k] - rowbase; wkn[k] = ent_w[tn * 4 + k]; } } }
.LBB0_1240:
	s_add_i32 s9, s4, 0xffff8800
	s_cmpk_lt_i32 s4, 0x7800
	s_cselect_b32 s27, s5, 0
	s_cselect_b32 s26, s4, s9
	s_waitcnt vmcnt(4)
	v_ashrrev_i32_e32 v23, 31, v4
	v_mov_b32_e32 v22, v4
	s_cselect_b32 s9, s22, s20
	s_cselect_b32 s28, s21, s19
	s_lshl_b64 s[26:27], s[26:27], 11
	v_lshlrev_b64 v[22:23], 11, v[22:23]
	s_add_u32 s26, s28, s26
	v_ashrrev_i32_e32 v19, 31, v2
	v_mov_b32_e32 v18, v2
	v_ashrrev_i32_e32 v21, 31, v3
	v_mov_b32_e32 v20, v3
	v_lshl_add_u64 v[70:71], v[14:15], 0, v[22:23]
	v_ashrrev_i32_e32 v23, 31, v5
	v_mov_b32_e32 v22, v5
	s_addc_u32 s27, s9, s27
	v_lshlrev_b64 v[18:19], 11, v[18:19]
	v_lshlrev_b64 v[20:21], 11, v[20:21]
	v_lshlrev_b64 v[22:23], 11, v[22:23]
	v_lshl_add_u64 v[18:19], v[14:15], 0, v[18:19]
	v_lshl_add_u64 v[20:21], v[14:15], 0, v[20:21]
	v_lshl_add_u64 v[72:73], v[14:15], 0, v[22:23]
	global_load_dwordx2 v[52:53], v67, s[26:27] nt
	global_load_dwordx2 v[42:43], v67, s[26:27] offset:512 nt
	global_load_dwordx2 v[32:33], v67, s[26:27] offset:1024 nt
	global_load_dwordx2 v[22:23], v67, s[26:27] offset:1536 nt
	global_load_dwordx2 v[54:55], v[18:19], off nt
	global_load_dwordx2 v[44:45], v[18:19], off offset:512 nt
	global_load_dwordx2 v[34:35], v[18:19], off offset:1024 nt
	global_load_dwordx2 v[28:29], v[18:19], off offset:1536 nt
	global_load_dwordx2 v[56:57], v[20:21], off nt
	global_load_dwordx2 v[46:47], v[20:21], off offset:512 nt
	global_load_dwordx2 v[36:37], v[20:21], off offset:1024 nt
	global_load_dwordx2 v[30:31], v[20:21], off offset:1536 nt
	global_load_dwordx2 v[58:59], v[70:71], off nt
	global_load_dwordx2 v[48:49], v[70:71], off offset:512 nt
	global_load_dwordx2 v[38:39], v[70:71], off offset:1024 nt
	global_load_dwordx2 v[24:25], v[70:71], off offset:1536 nt
	global_load_dwordx2 v[60:61], v[72:73], off nt
	global_load_dwordx2 v[50:51], v[72:73], off offset:512 nt
	global_load_dwordx2 v[40:41], v[72:73], off offset:1024 nt
	global_load_dwordx2 v[26:27], v[72:73], off offset:1536 nt
	s_add_i32 s9, s6, s4
	s_cmp_ge_i32 s9, s14
	s_waitcnt vmcnt(24)
	v_mov_b64_e32 v[20:21], v[6:7]
	v_mov_b64_e32 v[18:19], v[8:9]
	s_cbranch_scc1 .LBB0_1239
	s_add_i32 s26, s8, -3
	s_ashr_i32 s27, s26, 31
	s_lshl_b64 s[26:27], s[26:27], 2
	s_add_u32 s28, s15, s26
	s_addc_u32 s29, s16, s27
	s_add_u32 s26, s17, s26
	s_addc_u32 s27, s18, s27
	s_add_i32 s34, s8, -2
	s_ashr_i32 s35, s34, 31
	s_lshl_b64 s[34:35], s[34:35], 2
	s_add_u32 s36, s15, s34
	s_addc_u32 s37, s16, s35
	s_add_u32 s34, s17, s34
	s_addc_u32 s35, s18, s35
	s_add_i32 s38, s8, -1
	s_ashr_i32 s39, s38, 31
	s_lshl_b64 s[38:39], s[38:39], 2
	s_add_u32 s40, s15, s38
	s_addc_u32 s41, s16, s39
	s_add_u32 s38, s17, s38
	s_addc_u32 s39, s18, s39
	s_ashr_i32 s9, s8, 31
	s_lshl_b64 s[42:43], s[8:9], 2
	s_add_u32 s44, s15, s42
	s_addc_u32 s45, s16, s43
	s_add_u32 s42, s17, s42
	s_addc_u32 s43, s18, s43
	global_load_dword v2, v11, s[28:29]
	global_load_dword v20, v11, s[26:27]
	global_load_dword v3, v11, s[36:37]
	global_load_dword v21, v11, s[34:35]
	global_load_dword v4, v11, s[40:41]
	global_load_dword v18, v11, s[38:39]
	global_load_dword v5, v11, s[44:45]
	global_load_dword v19, v11, s[42:43]
	s_branch .LBB0_1239

; __device__ __forceinline__ void p_final(const Args& a, const Frame& F, int half) {
;     ...
;         f32x4* xr = (f32x4*)(a.out + (size_t)t * D) + F.lane;
;         const u32x2* x1p = (const u32x2*)x1_row(a.out, a.ws, t) + F.lane;
;         const f32x4* g2 = (const f32x4*)(mod + (t >> 13) * 6144 + 5120) + F.lane;
;         int rk[4]; float wk[4];
; #pragma unroll
;         for (int k = 0; k < 4; ++k) { rk[k] = rkn[k]; wk[k] = wkn[k]; }
;         u32x2 ok[4][4], xw[4];
; #pragma unroll
;         for (int j = 0; j < 4; ++j) { xw[j] = x1p[64 * j];
; #pragma unroll
;             for (int k = 0; k < 4; ++k) ok[j][k] = *((const u32x2*)(OUTK + (size_t)rk[k] * D) + F.lane + 64 * j); }
;         { const int tn = t + NGW; if (tn < tend) {
; #pragma unroll
;             for (int k = 0; k < 4; ++k) { rkn[k] = tok_row[tn * 4 + k] - rowbase; wkn[k] = ent_w[tn * 4 + k]; } } }
.LBB0_1396:
	s_add_i32 s7, s0, 0xffff8800
	s_cmpk_lt_i32 s0, 0x7800
	s_cselect_b32 s23, s1, 0
	s_cselect_b32 s22, s0, s7
	v_ashrrev_i32_e32 v21, 31, v14
	v_mov_b32_e32 v20, v14
	s_cselect_b32 s7, s18, s16
	s_cselect_b32 s21, s17, s15
	s_lshl_b64 s[22:23], s[22:23], 11
	v_lshlrev_b64 v[20:21], 11, v[20:21]
	s_add_u32 s22, s21, s22
	v_ashrrev_i32_e32 v17, 31, v12
	v_mov_b32_e32 v16, v12
	v_ashrrev_i32_e32 v19, 31, v13
	v_mov_b32_e32 v18, v13
	v_lshl_add_u64 v[70:71], v[8:9], 0, v[20:21]
	v_ashrrev_i32_e32 v21, 31, v15
	v_mov_b32_e32 v20, v15
	s_addc_u32 s23, s7, s23
	v_lshlrev_b64 v[16:17], 11, v[16:17]
	v_lshlrev_b64 v[18:19], 11, v[18:19]
	v_lshlrev_b64 v[20:21], 11, v[20:21]
	v_lshl_add_u64 v[16:17], v[8:9], 0, v[16:17]
	v_lshl_add_u64 v[18:19], v[8:9], 0, v[18:19]
	v_lshl_add_u64 v[72:73], v[8:9], 0, v[20:21]
	global_load_dwordx2 v[50:51], v60, s[22:23] nt
	global_load_dwordx2 v[40:41], v60, s[22:23] offset:512 nt
	global_load_dwordx2 v[30:31], v60, s[22:23] offset:1024 nt
	global_load_dwordx2 v[20:21], v60, s[22:23] offset:1536 nt
	global_load_dwordx2 v[52:53], v[16:17], off nt
	global_load_dwordx2 v[42:43], v[16:17], off offset:512 nt
	global_load_dwordx2 v[32:33], v[16:17], off offset:1024 nt
	global_load_dwordx2 v[26:27], v[16:17], off offset:1536 nt
	global_load_dwordx2 v[54:55], v[18:19], off nt
	global_load_dwordx2 v[44:45], v[18:19], off offset:512 nt
	global_load_dwordx2 v[34:35], v[18:19], off offset:1024 nt
	global_load_dwordx2 v[28:29], v[18:19], off offset:1536 nt
	global_load_dwordx2 v[56:57], v[70:71], off nt
	global_load_dwordx2 v[46:47], v[70:71], off offset:512 nt
	global_load_dwordx2 v[36:37], v[70:71], off offset:1024 nt
	global_load_dwordx2 v[22:23], v[70:71], off offset:1536 nt
	global_load_dwordx2 v[58:59], v[72:73], off nt
	global_load_dwordx2 v[48:49], v[72:73], off offset:512 nt
	global_load_dwordx2 v[38:39], v[72:73], off offset:1024 nt
	global_load_dwordx2 v[24:25], v[72:73], off offset:1536 nt
	s_add_i32 s7, s2, s0
	s_cmp_gt_i32 s7, 0xffff
	s_waitcnt vmcnt(24)
	v_mov_b64_e32 v[18:19], v[0:1]
	v_mov_b64_e32 v[16:17], v[2:3]
	s_cbranch_scc1 .LBB0_1395
	s_add_i32 s22, s6, -3
	s_ashr_i32 s23, s22, 31
	s_lshl_b64 s[22:23], s[22:23], 2
	s_add_u32 s24, s10, s22
	s_addc_u32 s25, s11, s23
	s_add_u32 s22, s12, s22
	s_addc_u32 s23, s13, s23
	s_add_i32 s26, s6, -2
	s_ashr_i32 s27, s26, 31
	s_lshl_b64 s[26:27], s[26:27], 2
	s_add_u32 s28, s10, s26
	s_addc_u32 s29, s11, s27
	s_add_u32 s26, s12, s26
	s_addc_u32 s27, s13, s27
	s_add_i32 s30, s6, -1
	s_ashr_i32 s31, s30, 31
	s_lshl_b64 s[30:31], s[30:31], 2
	s_add_u32 s34, s10, s30
	s_addc_u32 s35, s11, s31
	s_add_u32 s30, s12, s30
	s_addc_u32 s31, s13, s31
	s_ashr_i32 s7, s6, 31
	s_lshl_b64 s[36:37], s[6:7], 2
	s_add_u32 s38, s10, s36
	s_addc_u32 s39, s11, s37
	s_add_u32 s36, s12, s36
	s_addc_u32 s37, s13, s37
	global_load_dword v4, v5, s[24:25]
	global_load_dword v18, v5, s[22:23]
	global_load_dword v12, v5, s[28:29]
	global_load_dword v19, v5, s[26:27]
	global_load_dword v14, v5, s[34:35]
	global_load_dword v16, v5, s[30:31]
	global_load_dword v15, v5, s[38:39]
	global_load_dword v17, v5, s[36:37]
	s_waitcnt vmcnt(5)
	v_sub_u32_e32 v13, v12, v61
	v_sub_u32_e32 v12, v4, v61
	s_waitcnt vmcnt(3)
	v_sub_u32_e32 v14, v14, v61
	s_waitcnt vmcnt(1)
	v_sub_u32_e32 v15, v15, v61
	s_branch .LBB0_1395
